# attention phase: prefetched K chunk loaded straight into final registers, premature vmcnt waits removed
# baseline (speedup 1.0000x reference)
.LBB0_1050:
	s_mov_b32 s45, s13
	s_lshl_b32 s92, s40, 1
	s_lshl_b64 s[6:7], s[44:45], 12
	s_add_i32 s91, s91, s34
	s_cmpk_lt_i32 s91, 0x400
	s_cselect_b64 s[4:5], -1, 0
	s_cmpk_gt_i32 s91, 0x3ff
	s_cselect_b64 s[16:17], -1, 0
	s_lshl_b32 s12, s66, 7
	v_bitop3_b32 v2, s12, v153, v177 bitop3:0xce
	v_lshl_or_b32 v2, v2, 8, v170
	v_add_u32_e32 v3, 0, v2
	v_add_u32_e32 v2, s88, v2
	s_barrier
	s_waitcnt vmcnt(2)
	ds_write_b128 v2, v[18:21]
	v_bitop3_b32 v2, s12, v171, v177 bitop3:0xce
	v_lshl_or_b32 v2, v2, 8, v172
	s_and_b32 s2, s12, 0x80
	ds_write_b128 v3, v[34:37]
	v_add_u32_e32 v3, 0, v2
	v_add_u32_e32 v2, s88, v2
	s_lshl_b32 s10, 0xc00, s92
	s_waitcnt vmcnt(0)
	ds_write_b128 v2, v[22:25]
	v_bitop3_b32 v2, s12, v173, v177 bitop3:0xce
	s_add_u32 s18, s6, s41
	v_lshl_or_b32 v2, v2, 8, v170
	s_addc_u32 s19, s7, 0
	s_lshl_b32 s22, s50, 8
	ds_write_b128 v3, v[38:41]
	v_add_u32_e32 v3, 0, v2
	v_add_u32_e32 v2, s88, v2
	s_add_u32 s20, s3, s22
	ds_write_b128 v2, v[26:29]
	v_bitop3_b32 v2, s12, v174, v177 bitop3:0xce
	s_addc_u32 s21, s35, 0
	s_lshl_b64 s[6:7], s[12:13], s92
	v_lshl_or_b32 v2, v2, 8, v179
	s_add_u32 s6, s6, s18
	ds_write_b128 v3, v[42:45]
	v_add_u32_e32 v3, 0, v2
	v_add_u32_e32 v2, s88, v2
	s_addc_u32 s7, s7, s19
	ds_write_b128 v2, v[30:33]
	v_mul_lo_u32 v2, s10, v153
	s_mulk_i32 s7, 0x1800
	s_mul_hi_u32 s10, s6, 0x1800
	s_add_i32 s10, s10, s7
	s_mulk_i32 s6, 0x1800
	s_add_u32 s6, s20, s6
	s_addc_u32 s7, s21, s10
	s_or_b32 s10, s12, 32
	s_mov_b32 s11, s13
	s_lshl_b64 s[10:11], s[10:11], s92
	s_add_u32 s10, s10, s18
	v_or_b32_e32 v2, v2, v154
	s_addc_u32 s11, s11, s19
	v_lshlrev_b32_e32 v128, 1, v2
	v_mov_b32_e32 v129, v10
	s_mulk_i32 s11, 0x1800
	s_mul_hi_u32 s23, s10, 0x1800
	ds_write_b128 v3, v[46:49]
	v_lshl_add_u64 v[2:3], s[6:7], 0, v[128:129]
	s_add_i32 s23, s23, s11
	s_mulk_i32 s10, 0x1800
	v_add_co_u32_e32 v2, vcc, s89, v2
	s_add_u32 s10, s20, s10
	s_nop 0
	v_addc_co_u32_e32 v3, vcc, 0, v3, vcc
	s_addc_u32 s11, s21, s23
	global_load_dwordx4 v[18:21], v[2:3], off
	v_lshl_add_u64 v[2:3], s[10:11], 0, v[128:129]
	v_add_co_u32_e32 v2, vcc, s89, v2
	s_nop 1
	v_addc_co_u32_e32 v3, vcc, 0, v3, vcc
	global_load_dwordx4 v[22:25], v[2:3], off
	global_load_dwordx4 v[34:37], v128, s[6:7] offset:2048
	global_load_dwordx4 v[38:41], v128, s[10:11] offset:2048
	s_or_b32 s6, s12, 64
	s_mov_b32 s7, s13
	s_lshl_b64 s[6:7], s[6:7], s92
	s_add_u32 s6, s6, s18
	s_addc_u32 s7, s7, s19
	s_mulk_i32 s7, 0x1800
	s_mul_hi_u32 s10, s6, 0x1800
	s_add_i32 s10, s10, s7
	s_mulk_i32 s6, 0x1800
	s_add_u32 s6, s20, s6
	s_addc_u32 s7, s21, s10
	v_lshl_add_u64 v[2:3], s[6:7], 0, v[128:129]
	v_add_co_u32_e32 v2, vcc, s89, v2
	global_load_dwordx4 v[42:45], v128, s[6:7] offset:2048
	s_nop 0
	v_addc_co_u32_e32 v3, vcc, 0, v3, vcc
	global_load_dwordx4 v[26:29], v[2:3], off
	s_or_b32 s6, s12, 0x60
	s_mov_b32 s7, s13
	s_lshl_b64 s[6:7], s[6:7], s92
	s_add_u32 s6, s6, s18
	s_addc_u32 s7, s7, s19
	s_mulk_i32 s7, 0x1800
	s_mul_hi_u32 s10, s6, 0x1800
	s_add_i32 s10, s10, s7
	s_mulk_i32 s6, 0x1800
	s_add_u32 s6, s20, s6
	s_addc_u32 s7, s21, s10
	v_lshl_add_u64 v[2:3], s[6:7], 0, v[128:129]
	v_add_co_u32_e32 v2, vcc, s89, v2
	global_load_dwordx4 v[46:49], v128, s[6:7] offset:2048
	s_nop 0
	v_addc_co_u32_e32 v3, vcc, 0, v3, vcc
	global_load_dwordx4 v[30:33], v[2:3], off
	s_lshl_b32 s6, 0x1800, s92
	v_mul_lo_u32 v2, s6, v206
	s_add_i32 s6, s12, s62
	s_mov_b32 s7, s13
	s_lshl_b64 s[6:7], s[6:7], s92
	s_add_u32 s6, s6, s18
	s_addc_u32 s7, s7, s19
	s_mulk_i32 s7, 0x1800
	s_mul_hi_u32 s10, s6, 0x1800
	s_add_i32 s10, s10, s7
	s_mulk_i32 s6, 0x1800
	s_add_u32 s6, s3, s6
	s_addc_u32 s7, s35, s10
	s_add_u32 s6, s6, s22
	v_or_b32_e32 v66, v2, v167
	s_addc_u32 s7, s7, 0
	global_load_dwordx4 v[62:65], v66, s[6:7] offset:192
	global_load_dwordx4 v[58:61], v66, s[6:7] offset:128
	global_load_dwordx4 v[54:57], v66, s[6:7] offset:64
	global_load_dwordx4 v[50:53], v66, s[6:7]
	s_add_i32 s6, s91, 0xfffffe00
	s_and_b32 s10, s91, 7
	s_lshl_b32 s23, s91, 2
	s_lshr_b32 s6, s6, 7
	s_and_b32 s7, s91, 15
	s_bfe_u32 s11, s91, 0x20006
	s_bfe_u32 s22, s91, 0x20001
	s_and_b32 s23, s23, 4
	s_lshl_b32 s10, s10, 2
	s_cmpk_lt_u32 s91, 0x100
	s_cselect_b32 s24, 0, s22
	s_cselect_b32 s45, s10, s23
	s_min_i32 s10, s91, 0x200
	s_ashr_i32 s93, s10, 8
	s_cmpk_lt_i32 s91, 0x200
	s_cselect_b32 s22, s11, s6
	s_cselect_b32 s6, 3, 4
	s_cselect_b32 s94, s24, s7
	s_cselect_b32 s10, s45, 0
	s_cselect_b32 s95, 4, 2
	s_lshr_b32 s6, s91, s6
	s_mov_b32 s23, s13
	s_and_b32 s96, s6, 7
	s_lshl_b64 s[6:7], s[22:23], 12
	s_lshl_b32 s23, s93, 1
	s_lshl_b32 s11, 0xc00, s23
	s_cmp_lg_u32 s10, 0
	s_cselect_b64 s[24:25], -1, 0
	s_lshl_b32 s26, s10, 7
	v_mul_lo_u32 v2, s11, v153
	s_add_i32 s10, s26, 0xffffff80
	s_or_b32 s6, s6, s94
	s_lshl_b32 s11, s96, 8
	s_add_u32 s27, s3, s11
	s_mov_b32 s11, s13
	s_addc_u32 s33, s35, 0
	s_lshl_b64 s[10:11], s[10:11], s23
	s_add_u32 s10, s10, s6
	s_addc_u32 s11, s11, s7
	s_mulk_i32 s11, 0x1800
	s_mul_hi_u32 s51, s10, 0x1800
	s_add_i32 s51, s51, s11
	s_mulk_i32 s10, 0x1800
	v_or_b32_e32 v2, v2, v154
	s_add_u32 s10, s27, s10
	v_lshlrev_b32_e32 v2, 1, v2
	v_mov_b32_e32 v3, v10
	s_addc_u32 s11, s33, s51
	v_lshl_add_u64 v[130:131], s[10:11], 0, v[2:3]
	s_add_i32 s10, s26, 0xffffffa0
	s_mov_b32 s11, s13
	s_lshl_b64 s[10:11], s[10:11], s23
	s_add_u32 s10, s10, s6
	s_addc_u32 s11, s11, s7
	s_mulk_i32 s11, 0x1800
	s_mul_hi_u32 s51, s10, 0x1800
	s_add_i32 s51, s51, s11
	s_mulk_i32 s10, 0x1800
	s_add_u32 s10, s27, s10
	s_addc_u32 s11, s33, s51
	v_lshl_add_u64 v[134:135], s[10:11], 0, v[2:3]
	s_sub_i32 s10, s26, 64
	s_mov_b32 s11, s13
	s_lshl_b64 s[10:11], s[10:11], s23
	s_add_u32 s10, s10, s6
	s_addc_u32 s11, s11, s7
	s_mulk_i32 s11, 0x1800
	s_mul_hi_u32 s51, s10, 0x1800
	s_add_i32 s51, s51, s11
	s_mulk_i32 s10, 0x1800
	s_add_u32 s10, s27, s10
	s_addc_u32 s11, s33, s51
	v_lshl_add_u64 v[138:139], s[10:11], 0, v[2:3]
	s_sub_i32 s10, s26, 32
	s_mov_b32 s11, s13
	s_lshl_b64 s[10:11], s[10:11], s23
	s_add_u32 s6, s10, s6
	s_addc_u32 s7, s11, s7
	s_mulk_i32 s7, 0x1800
	s_mul_hi_u32 s10, s6, 0x1800
	s_add_i32 s10, s10, s7
	s_mulk_i32 s6, 0x1800
	s_add_u32 s6, s27, s6
	s_addc_u32 s7, s33, s10
	v_lshl_add_u64 v[142:143], s[6:7], 0, v[2:3]
	v_or_b32_e32 v2, s2, v153
	v_lshl_or_b32 v2, v2, 8, v170
	v_add_u32_e32 v3, 0, v2
	v_add_u32_e32 v2, s88, v2
	s_waitcnt vmcnt(11)
	ds_write_b128 v2, v[18:21]
	v_or_b32_e32 v2, s2, v171
	v_lshl_or_b32 v2, v2, 8, v172
	s_waitcnt vmcnt(9)
	ds_write_b128 v3, v[34:37]
	v_add_u32_e32 v3, 0, v2
	v_add_u32_e32 v2, s88, v2
	ds_write_b128 v2, v[22:25]
	v_or_b32_e32 v2, s2, v173
	v_lshl_or_b32 v2, v2, 8, v170
	s_waitcnt vmcnt(8)
	ds_write_b128 v3, v[38:41]
	v_add_u32_e32 v3, 0, v2
	v_add_u32_e32 v2, s88, v2
	s_waitcnt vmcnt(6)
	ds_write_b128 v2, v[26:29]
	v_or_b32_e32 v2, s2, v174
	v_lshl_or_b32 v2, v2, 8, v179
	ds_write_b128 v3, v[42:45]
	v_add_u32_e32 v3, 0, v2
	v_add_u32_e32 v2, s88, v2
	s_cmp_gt_i32 s59, 1
	s_waitcnt vmcnt(4)
	ds_write_b128 v2, v[30:33]
	s_cselect_b64 s[52:53], -1, 0
	v_cndmask_b32_e64 v2, 0, 1, s[4:5]
	v_lshl_add_u64 v[132:133], v[130:131], 0, s[14:15]
	v_lshl_add_u64 v[136:137], v[134:135], 0, s[14:15]
	v_lshl_add_u64 v[140:141], v[138:139], 0, s[14:15]
	v_lshl_add_u64 v[144:145], v[142:143], 0, s[14:15]
	s_mov_b64 s[6:7], -1
	s_and_b64 vcc, exec, s[52:53]
	v_cmp_ne_u32_e64 s[4:5], 1, v2
	ds_write_b128 v3, v[46:49]
	s_waitcnt vmcnt(0) lgkmcnt(0)
	s_barrier
	s_cbranch_vccnz .LBB0_1060
	s_and_b64 vcc, exec, s[4:5]
	s_mov_b32 s56, s40
	s_mov_b32 s57, s44
	s_mov_b32 s97, s50
	s_mov_b32 s33, s41
	s_mov_b32 s58, s66
	s_mov_b32 s10, s59
	s_cbranch_vccnz .LBB0_1059
	v_cndmask_b32_e64 v2, 0, 1, s[24:25]
	v_cmp_ne_u32_e64 s[6:7], 1, v2
	s_andn2_b64 vcc, exec, s[24:25]
	s_cbranch_vccnz .LBB0_1105
	global_load_dwordx4 v[34:37], v[130:131], off offset:2048
	global_load_dwordx4 v[2:5], v[132:133], off
	global_load_dwordx4 v[38:41], v[134:135], off offset:2048
	global_load_dwordx4 v[6:9], v[136:137], off
	s_cbranch_execnz .LBB0_1055

.LBB0_1063:
	s_add_i32 s6, s12, 0x80
	v_mov_b32_e32 v18, 0
	s_andn2_b64 vcc, exec, s[56:57]
	v_mov_b32_e32 v19, 0
	v_mov_b32_e32 v20, 0
	v_mov_b32_e32 v21, 0
	v_mov_b32_e32 v22, 0
	v_mov_b32_e32 v23, 0
	v_mov_b32_e32 v24, 0
	v_mov_b32_e32 v25, 0
	v_mov_b32_e32 v2, 0
	v_mov_b32_e32 v3, 0
	v_mov_b32_e32 v4, 0
	v_mov_b32_e32 v5, 0
	v_mov_b32_e32 v6, 0
	v_mov_b32_e32 v7, 0
	v_mov_b32_e32 v8, 0
	v_mov_b32_e32 v9, 0
	s_cbranch_vccnz .LBB0_1065
	s_mov_b32 s7, s13
	s_lshl_b64 s[10:11], s[6:7], s92
	s_add_u32 s2, s10, s18
	s_addc_u32 s7, s11, s19
	s_mulk_i32 s7, 0x1800
	s_mul_hi_u32 s10, s2, 0x1800
	s_add_i32 s7, s10, s7
	s_mulk_i32 s2, 0x1800
	s_add_u32 s10, s20, s2
	s_addc_u32 s11, s21, s7
	v_lshl_add_u64 v[2:3], s[10:11], 0, v[128:129]
	s_or_b32 s10, s6, 32
	s_mov_b32 s11, s13
	s_lshl_b64 s[10:11], s[10:11], s92
	s_add_u32 s2, s10, s18
	s_addc_u32 s7, s11, s19
	s_mulk_i32 s7, 0x1800
	s_mul_hi_u32 s10, s2, 0x1800
	s_add_i32 s7, s10, s7
	s_mulk_i32 s2, 0x1800
	v_add_co_u32_e32 v6, vcc, s89, v2
	s_add_u32 s10, s20, s2
	s_nop 0
	v_addc_co_u32_e32 v7, vcc, 0, v3, vcc
	s_addc_u32 s11, s21, s7
	global_load_dwordx4 v[34:37], v[2:3], off offset:2048
	s_nop 0
	global_load_dwordx4 v[18:21], v[6:7], off
	v_lshl_add_u64 v[6:7], s[10:11], 0, v[128:129]
	v_add_co_u32_e32 v12, vcc, s89, v6
	s_nop 1
	v_addc_co_u32_e32 v13, vcc, 0, v7, vcc
	global_load_dwordx4 v[38:41], v[6:7], off offset:2048
	s_nop 0
	global_load_dwordx4 v[22:25], v[12:13], off

.LBB0_1067:
	s_andn2_b64 vcc, exec, s[54:55]
	s_cbranch_vccnz .LBB0_1069
	s_or_b32 s10, s6, 64
	s_mov_b32 s11, s13
	s_lshl_b64 s[10:11], s[10:11], s92
	s_add_u32 s2, s10, s18
	s_addc_u32 s7, s11, s19
	s_mulk_i32 s7, 0x1800
	s_mul_hi_u32 s10, s2, 0x1800
	s_add_i32 s7, s10, s7
	s_mulk_i32 s2, 0x1800
	s_add_u32 s10, s20, s2
	s_addc_u32 s11, s21, s7
	v_lshl_add_u64 v[26:27], s[10:11], 0, v[128:129]
	global_load_dwordx4 v[42:45], v[26:27], off offset:2048
	s_or_b32 s6, s6, 0x60
	s_mov_b32 s7, s13
	s_lshl_b64 s[6:7], s[6:7], s92
	s_add_u32 s2, s6, s18
	s_addc_u32 s6, s7, s19
	s_mulk_i32 s6, 0x1800
	s_mul_hi_u32 s7, s2, 0x1800
	s_add_i32 s7, s7, s6
	s_mulk_i32 s2, 0x1800
	s_add_u32 s6, s20, s2
	v_add_co_u32_e32 v26, vcc, s89, v26
	s_addc_u32 s7, s21, s7
	s_nop 0
	v_addc_co_u32_e32 v27, vcc, 0, v27, vcc
	global_load_dwordx4 v[26:29], v[26:27], off
	v_lshl_add_u64 v[2:3], s[6:7], 0, v[128:129]
	global_load_dwordx4 v[46:49], v[2:3], off offset:2048
	v_add_co_u32_e32 v2, vcc, 0x1000, v2
	s_nop 1
	v_addc_co_u32_e32 v3, vcc, 0, v3, vcc
	global_load_dwordx4 v[30:33], v[2:3], off

.LBB0_1070:
	s_lshl_b32 s11, s66, 3
	s_andn2_b32 s7, 8, s11
	s_xor_b32 s2, s7, s63
	s_lshl_b32 s27, s2, 12
	s_add_i32 s2, s27, 0
	v_add_u32_e32 v11, s2, v157
	v_add_u32_e32 v2, s2, v155
	v_add_u32_e32 v6, s2, v156
	ds_read_b128 v[12:15], v11
	v_add_u32_e32 v11, s2, v158
	s_xor_b32 s2, s7, s65
	s_lshl_b32 s51, s2, 12
	v_mov_b32_e32 v67, v10
	s_add_i32 s2, s51, 0
	v_lshl_add_u64 v[146:147], s[20:21], 0, v[66:67]
	ds_read_b128 v[66:69], v11
	v_add_u32_e32 v11, s2, v155
	ds_read_b128 v[70:73], v11
	v_add_u32_e32 v11, s2, v156
	ds_read_b128 v[74:77], v11
	v_add_u32_e32 v11, s2, v157
	ds_read_b128 v[78:81], v11
	v_add_u32_e32 v11, s2, v158
	s_xor_b32 s2, s7, s64
	s_lshl_b32 s60, s2, 12
	s_add_i32 s2, s60, 0
	ds_read_b128 v[82:85], v11
	v_add_u32_e32 v11, s2, v155
	ds_read_b128 v[90:93], v11
	v_add_u32_e32 v11, s2, v156
	ds_read_b128 v[94:97], v11
	v_add_u32_e32 v11, s2, v157
	ds_read_b128 v[102:105], v11
	v_add_u32_e32 v11, s2, v158
	s_xor_b32 s2, s7, s67
	s_lshl_b32 s26, s2, 12
	s_add_i32 s2, s26, 0
	ds_read_b128 v[106:109], v11
	v_add_u32_e32 v11, s2, v155
	ds_read_b128 v[114:117], v11
	v_add_u32_e32 v11, s2, v156
	ds_read_b128 v[118:121], v11
	v_add_u32_e32 v11, s2, v157
	ds_read_b128 v[2:5], v2
	ds_read_b128 v[6:9], v6
	ds_read_b128 v[122:125], v11
	v_add_u32_e32 v11, s2, v158
	ds_read_b128 v[182:185], v11
	s_lshl_b32 s23, s50, 7
	s_waitcnt lgkmcnt(3)
	v_mfma_f32_16x16x32_bf16 v[2:5], v[2:5], v[50:53], 0
	s_waitcnt lgkmcnt(2)
	v_mfma_f32_16x16x32_bf16 v[2:5], v[6:9], v[54:57], v[2:5]
	v_mfma_f32_16x16x32_bf16 v[2:5], v[12:15], v[58:61], v[2:5]
	v_mfma_f32_16x16x32_bf16 v[98:101], v[66:69], v[62:65], v[2:5]
	v_mfma_f32_16x16x32_bf16 v[2:5], v[70:73], v[50:53], 0
	v_mfma_f32_16x16x32_bf16 v[2:5], v[74:77], v[54:57], v[2:5]
	v_mfma_f32_16x16x32_bf16 v[2:5], v[78:81], v[58:61], v[2:5]
	v_mfma_f32_16x16x32_bf16 v[86:89], v[82:85], v[62:65], v[2:5]
	s_xor_b32 s2, s7, s70
	s_lshl_b32 s61, s2, 12
	s_add_i32 s2, s61, 0
	s_nop 3
	v_add_u32_e32 v2, s2, v155
	v_add_u32_e32 v6, s2, v156
	v_add_u32_e32 v11, s2, v157
	v_add_u32_e32 v16, s2, v158
	s_xor_b32 s2, s7, s71
	s_lshl_b32 s2, s2, 12
	s_add_i32 s6, s2, 0
	ds_read_b128 v[2:5], v2
	ds_read_b128 v[6:9], v6
	ds_read_b128 v[12:15], v11
	ds_read_b128 v[66:69], v16
	v_add_u32_e32 v11, s6, v155
	v_add_u32_e32 v16, s6, v156
	ds_read_b128 v[70:73], v11
	ds_read_b128 v[74:77], v16
	v_add_u32_e32 v11, s6, v157
	v_add_u32_e32 v16, s6, v158
	ds_read_b128 v[78:81], v11
	ds_read_b128 v[82:85], v16
	v_mfma_f32_16x16x32_bf16 v[90:93], v[90:93], v[50:53], 0
	v_mfma_f32_16x16x32_bf16 v[90:93], v[94:97], v[54:57], v[90:93]
	v_mfma_f32_16x16x32_bf16 v[90:93], v[102:105], v[58:61], v[90:93]
	v_mfma_f32_16x16x32_bf16 v[110:113], v[106:109], v[62:65], v[90:93]
	v_mfma_f32_16x16x32_bf16 v[90:93], v[114:117], v[50:53], 0
	v_mfma_f32_16x16x32_bf16 v[90:93], v[118:121], v[54:57], v[90:93]
	s_waitcnt lgkmcnt(9)
	v_mfma_f32_16x16x32_bf16 v[90:93], v[122:125], v[58:61], v[90:93]
	s_waitcnt lgkmcnt(8)
	v_mfma_f32_16x16x32_bf16 v[94:97], v[182:185], v[62:65], v[90:93]
	s_xor_b32 s6, s7, s74
	s_lshl_b32 s54, s6, 12
	s_add_i32 s6, s54, 0
	v_add_u32_e32 v11, s6, v155
	v_add_u32_e32 v16, s6, v156
	s_nop 0
	ds_read_b128 v[90:93], v11
	ds_read_b128 v[106:109], v16
	v_add_u32_e32 v11, s6, v157
	v_add_u32_e32 v16, s6, v158
	s_xor_b32 s6, s7, s75
	s_lshl_b32 s55, s6, 12
	s_add_i32 s6, s55, 0
	ds_read_b128 v[118:121], v11
	ds_read_b128 v[122:125], v16
	v_add_u32_e32 v11, s6, v155
	v_add_u32_e32 v16, s6, v156
	ds_read_b128 v[182:185], v11
	ds_read_b128 v[186:189], v16
	v_add_u32_e32 v11, s6, v157
	v_add_u32_e32 v16, s6, v158
	ds_read_b128 v[190:193], v11
	ds_read_b128 v[194:197], v16
	s_waitcnt lgkmcnt(14)
	v_mfma_f32_16x16x32_bf16 v[2:5], v[2:5], v[50:53], 0
	v_mfma_f32_16x16x32_bf16 v[2:5], v[6:9], v[54:57], v[2:5]
	s_waitcnt lgkmcnt(13)
	v_mfma_f32_16x16x32_bf16 v[2:5], v[12:15], v[58:61], v[2:5]
	s_waitcnt lgkmcnt(12)
	v_mfma_f32_16x16x32_bf16 v[114:117], v[66:69], v[62:65], v[2:5]
	s_waitcnt lgkmcnt(11)
	v_mfma_f32_16x16x32_bf16 v[2:5], v[70:73], v[50:53], 0
	s_waitcnt lgkmcnt(10)
	v_mfma_f32_16x16x32_bf16 v[2:5], v[74:77], v[54:57], v[2:5]
	s_waitcnt lgkmcnt(9)
	v_mfma_f32_16x16x32_bf16 v[2:5], v[78:81], v[58:61], v[2:5]
	s_waitcnt lgkmcnt(8)
	v_mfma_f32_16x16x32_bf16 v[102:105], v[82:85], v[62:65], v[2:5]
	s_xor_b32 s6, s7, s82
	s_lshl_b32 s6, s6, 12
	s_xor_b32 s7, s7, s83
	s_add_i32 vcc_lo, s6, 0
	s_lshl_b32 s7, s7, 12
	s_nop 0
	v_add_u32_e32 v2, vcc_lo, v155
	v_add_u32_e32 v6, vcc_lo, v156
	v_add_u32_e32 v11, vcc_lo, v157
	v_add_u32_e32 v16, vcc_lo, v158
	s_add_i32 vcc_lo, s7, 0
	ds_read_b128 v[2:5], v2
	ds_read_b128 v[6:9], v6
	ds_read_b128 v[12:15], v11
	ds_read_b128 v[66:69], v16
	v_add_u32_e32 v11, vcc_lo, v155
	v_add_u32_e32 v16, vcc_lo, v156
	ds_read_b128 v[70:73], v11
	ds_read_b128 v[74:77], v16
	v_add_u32_e32 v11, vcc_lo, v157
	v_add_u32_e32 v16, vcc_lo, v158
	ds_read_b128 v[78:81], v11
	ds_read_b128 v[82:85], v16
	s_waitcnt lgkmcnt(14)
	v_mfma_f32_16x16x32_bf16 v[90:93], v[90:93], v[50:53], 0
	v_mfma_f32_16x16x32_bf16 v[90:93], v[106:109], v[54:57], v[90:93]
	s_waitcnt lgkmcnt(13)
	v_mfma_f32_16x16x32_bf16 v[90:93], v[118:121], v[58:61], v[90:93]
	s_waitcnt lgkmcnt(12)
	v_mfma_f32_16x16x32_bf16 v[122:125], v[122:125], v[62:65], v[90:93]
	s_waitcnt lgkmcnt(11)
	v_mfma_f32_16x16x32_bf16 v[90:93], v[182:185], v[50:53], 0
	s_waitcnt lgkmcnt(10)
	v_mfma_f32_16x16x32_bf16 v[90:93], v[186:189], v[54:57], v[90:93]
	s_waitcnt lgkmcnt(9)
	v_mfma_f32_16x16x32_bf16 v[90:93], v[190:193], v[58:61], v[90:93]
	s_waitcnt lgkmcnt(8)
	v_mfma_f32_16x16x32_bf16 v[118:121], v[194:197], v[62:65], v[90:93]
	s_waitcnt lgkmcnt(7)
	v_mfma_f32_16x16x32_bf16 v[2:5], v[2:5], v[50:53], 0
	s_waitcnt lgkmcnt(6)
	v_mfma_f32_16x16x32_bf16 v[2:5], v[6:9], v[54:57], v[2:5]
	s_waitcnt lgkmcnt(5)
	v_mfma_f32_16x16x32_bf16 v[2:5], v[12:15], v[58:61], v[2:5]
	s_waitcnt lgkmcnt(4)
	v_mfma_f32_16x16x32_bf16 v[106:109], v[66:69], v[62:65], v[2:5]
	s_waitcnt lgkmcnt(3)
	v_mfma_f32_16x16x32_bf16 v[2:5], v[70:73], v[50:53], 0
	s_waitcnt lgkmcnt(2)
	v_mfma_f32_16x16x32_bf16 v[2:5], v[74:77], v[54:57], v[2:5]
	s_waitcnt lgkmcnt(1)
	v_mfma_f32_16x16x32_bf16 v[2:5], v[78:81], v[58:61], v[2:5]
	s_waitcnt lgkmcnt(0)
	v_mfma_f32_16x16x32_bf16 v[90:93], v[82:85], v[62:65], v[2:5]
	s_add_i32 s27, s88, s27
	s_add_i32 s51, s88, s51
	s_nop 3
	v_add_u32_e32 v2, s27, v159
	v_add_u32_e32 v3, s51, v159
	v_add_u32_e32 v4, s27, v160
	v_add_u32_e32 v5, s51, v160
	v_add_u32_e32 v6, s27, v161
	v_add_u32_e32 v7, s51, v161
	v_add_u32_e32 v8, s27, v162
	v_add_u32_e32 v9, s51, v162
	v_add_u32_e32 v11, s27, v163
	v_add_u32_e32 v12, s51, v163
	v_add_u32_e32 v13, s27, v164
	v_add_u32_e32 v14, s51, v164
	ds_read_b64_tr_b16 v[70:71], v2
	ds_read_b64_tr_b16 v[72:73], v3
	ds_read_b64_tr_b16 v[2:3], v4
	ds_read_b64_tr_b16 v[4:5], v5
	ds_read_b64_tr_b16 v[74:75], v6
	ds_read_b64_tr_b16 v[76:77], v7
	ds_read_b64_tr_b16 v[6:7], v8
	ds_read_b64_tr_b16 v[8:9], v9
	ds_read_b64_tr_b16 v[78:79], v11
	ds_read_b64_tr_b16 v[80:81], v12
	ds_read_b64_tr_b16 v[12:13], v13
	ds_read_b64_tr_b16 v[14:15], v14
	v_add_u32_e32 v11, s27, v165
	v_add_u32_e32 v68, s51, v166
	v_add_u32_e32 v16, s51, v165
	v_add_u32_e32 v17, s27, v166
	ds_read_b64_tr_b16 v[82:83], v11
	ds_read_b64_tr_b16 v[84:85], v16
	ds_read_b64_tr_b16 v[66:67], v17
	ds_read_b64_tr_b16 v[68:69], v68
	s_andn2_b64 vcc, exec, s[52:53]
	s_cbranch_vccnz .LBB0_1072
	v_readlane_b32 s27, v253, 20
	s_add_i32 s52, s27, s12
	s_ashr_i32 s53, s52, 31
	s_lshl_b64 s[52:53], s[52:53], s92
	s_add_u32 s27, s52, s18
	s_addc_u32 s51, s53, s19
	s_mulk_i32 s51, 0x1800
	v_mad_u64_u32 v[16:17], s[52:53], s27, v180, v[146:147]
	v_add_u32_e32 v17, s51, v17
	global_load_dwordx4 v[50:53], v[16:17], off
	global_load_dwordx4 v[54:57], v[16:17], off offset:64
	global_load_dwordx4 v[58:61], v[16:17], off offset:128
	global_load_dwordx4 v[62:65], v[16:17], off offset:192

.LBB0_1076:
	s_add_i32 s6, s12, 0xffffff80
	s_and_b32 s6, s6, 0x80
	v_or_b32_e32 v2, s6, v153
	v_lshl_or_b32 v2, v2, 8, v170
	v_add_u32_e32 v3, 0, v2
	v_add_u32_e32 v2, s88, v2
	s_waitcnt vmcnt(8)
	s_barrier
	ds_write_b128 v2, v[18:21]
	v_or_b32_e32 v2, s6, v171
	v_lshl_or_b32 v2, v2, 8, v172
	ds_write_b128 v3, v[34:37]
	v_add_u32_e32 v3, 0, v2
	v_add_u32_e32 v2, s88, v2
	ds_write_b128 v2, v[22:25]
	v_or_b32_e32 v2, s6, v173
	v_lshl_or_b32 v2, v2, 8, v170
	ds_write_b128 v3, v[38:41]
	v_add_u32_e32 v3, 0, v2
	v_add_u32_e32 v2, s88, v2
	ds_write_b128 v2, v[26:29]
	v_or_b32_e32 v2, s6, v174
	v_lshlrev_b32_e32 v2, 8, v2
	s_add_i32 s51, s2, 1
	v_lshl_or_b32 v2, v178, 4, v2
	s_cmp_lt_i32 s51, s59
	ds_write_b128 v3, v[42:45]
	v_add_u32_e32 v3, 0, v2
	v_add_u32_e32 v2, s88, v2
	s_cselect_b64 s[54:55], -1, 0
	s_cmp_ge_i32 s51, s59
	s_mov_b64 s[6:7], -1
	ds_write_b128 v3, v[46:49]
	ds_write_b128 v2, v[30:33]
	s_waitcnt lgkmcnt(0)
	s_barrier
	s_cbranch_scc0 .LBB0_1086
	s_and_b64 vcc, exec, s[4:5]
	s_mov_b32 s40, s56
	s_mov_b32 s44, s57
	s_mov_b32 s50, s97
	s_mov_b32 s41, s33
	s_mov_b32 s23, s58
	s_mov_b32 s61, s10
	s_cbranch_vccnz .LBB0_1085
	v_cndmask_b32_e64 v2, 0, 1, s[24:25]
	v_cmp_ne_u32_e64 s[6:7], 1, v2
	s_andn2_b64 vcc, exec, s[24:25]
	s_cbranch_vccnz .LBB0_1102
	global_load_dwordx4 v[34:37], v[130:131], off offset:2048
	global_load_dwordx4 v[2:5], v[132:133], off
	global_load_dwordx4 v[38:41], v[134:135], off offset:2048
	global_load_dwordx4 v[6:9], v[136:137], off
	s_cbranch_execnz .LBB0_1081

.LBB0_1089:
	v_mov_b32_e32 v18, 0
	s_andn2_b64 vcc, exec, s[40:41]
	v_mov_b32_e32 v19, 0
	v_mov_b32_e32 v20, 0
	v_mov_b32_e32 v21, 0
	v_mov_b32_e32 v22, 0
	v_mov_b32_e32 v23, 0
	v_mov_b32_e32 v24, 0
	v_mov_b32_e32 v25, 0
	v_mov_b32_e32 v2, 0
	v_mov_b32_e32 v3, 0
	v_mov_b32_e32 v4, 0
	v_mov_b32_e32 v5, 0
	v_mov_b32_e32 v6, 0
	v_mov_b32_e32 v7, 0
	v_mov_b32_e32 v8, 0
	v_mov_b32_e32 v9, 0
	s_cbranch_vccnz .LBB0_1091
	s_lshl_b64 s[26:27], s[12:13], s92
	s_add_u32 s2, s26, s18
	s_addc_u32 s23, s27, s19
	s_mulk_i32 s23, 0x1800
	s_mul_hi_u32 s26, s2, 0x1800
	s_add_i32 s23, s26, s23
	s_mulk_i32 s2, 0x1800
	s_add_u32 s26, s20, s2
	s_addc_u32 s27, s21, s23
	v_lshl_add_u64 v[2:3], s[26:27], 0, v[128:129]
	s_add_i32 s26, s12, 32
	s_mov_b32 s27, s13
	s_lshl_b64 s[26:27], s[26:27], s92
	s_add_u32 s2, s26, s18
	s_addc_u32 s23, s27, s19
	s_mulk_i32 s23, 0x1800
	s_mul_hi_u32 s26, s2, 0x1800
	s_add_i32 s23, s26, s23
	s_mulk_i32 s2, 0x1800
	v_add_co_u32_e32 v6, vcc, s89, v2
	s_add_u32 s26, s20, s2
	s_nop 0
	v_addc_co_u32_e32 v7, vcc, 0, v3, vcc
	s_addc_u32 s27, s21, s23
	global_load_dwordx4 v[34:37], v[2:3], off offset:2048
	s_nop 0
	global_load_dwordx4 v[18:21], v[6:7], off
	v_lshl_add_u64 v[6:7], s[26:27], 0, v[128:129]
	v_add_co_u32_e32 v12, vcc, s89, v6
	s_nop 1
	v_addc_co_u32_e32 v13, vcc, 0, v7, vcc
	global_load_dwordx4 v[38:41], v[6:7], off offset:2048
	s_nop 0
	global_load_dwordx4 v[22:25], v[12:13], off

.LBB0_1093:
	s_andn2_b64 vcc, exec, s[40:41]
	s_cbranch_vccnz .LBB0_1095
	s_add_i32 s6, s12, 64
	s_mov_b32 s7, s13
	s_lshl_b64 s[6:7], s[6:7], s92
	s_add_u32 s2, s6, s18
	s_addc_u32 s6, s7, s19
	s_mulk_i32 s6, 0x1800
	s_mul_hi_u32 s7, s2, 0x1800
	s_add_i32 s7, s7, s6
	s_mulk_i32 s2, 0x1800
	s_add_u32 s6, s20, s2
	s_addc_u32 s7, s21, s7
	v_lshl_add_u64 v[26:27], s[6:7], 0, v[128:129]
	global_load_dwordx4 v[42:45], v[26:27], off offset:2048
	s_add_i32 s6, s12, 0x60
	s_mov_b32 s7, s13
	s_lshl_b64 s[6:7], s[6:7], s92
	s_add_u32 s2, s6, s18
	s_addc_u32 s6, s7, s19
	s_mulk_i32 s6, 0x1800
	s_mul_hi_u32 s7, s2, 0x1800
	s_add_i32 s7, s7, s6
	s_mulk_i32 s2, 0x1800
	s_add_u32 s6, s20, s2
	v_add_co_u32_e32 v26, vcc, s89, v26
	s_addc_u32 s7, s21, s7
	s_nop 0
	v_addc_co_u32_e32 v27, vcc, 0, v27, vcc
	global_load_dwordx4 v[26:29], v[26:27], off
	v_lshl_add_u64 v[2:3], s[6:7], 0, v[128:129]
	global_load_dwordx4 v[46:49], v[2:3], off offset:2048
	v_add_co_u32_e32 v2, vcc, 0x1000, v2
	s_nop 1
	v_addc_co_u32_e32 v3, vcc, 0, v3, vcc
	global_load_dwordx4 v[30:33], v[2:3], off

.LBB0_1096:
	s_andn2_b32 s7, 8, s11
	s_xor_b32 s2, s7, s63
	s_lshl_b32 s57, s2, 12
	s_add_i32 s2, s57, 0
	v_add_u32_e32 v2, s2, v155
	v_add_u32_e32 v6, s2, v156
	v_add_u32_e32 v11, s2, v157
	v_add_u32_e32 v16, s2, v158
	s_xor_b32 s2, s7, s65
	s_lshl_b32 s58, s2, 12
	s_add_i32 s2, s58, 0
	ds_read_b128 v[2:5], v2
	ds_read_b128 v[6:9], v6
	ds_read_b128 v[12:15], v11
	ds_read_b128 v[66:69], v16
	v_add_u32_e32 v11, s2, v155
	v_add_u32_e32 v16, s2, v156
	ds_read_b128 v[70:73], v11
	ds_read_b128 v[74:77], v16
	v_add_u32_e32 v11, s2, v157
	v_add_u32_e32 v16, s2, v158
	s_xor_b32 s2, s7, s64
	s_lshl_b32 s26, s2, 12
	s_add_i32 s2, s26, 0
	ds_read_b128 v[78:81], v11
	ds_read_b128 v[82:85], v16
	v_add_u32_e32 v11, s2, v155
	v_add_u32_e32 v16, s2, v156
	ds_read_b128 v[90:93], v11
	ds_read_b128 v[94:97], v16
	v_add_u32_e32 v11, s2, v157
	v_add_u32_e32 v16, s2, v158
	s_xor_b32 s2, s7, s67
	s_lshl_b32 s27, s2, 12
	s_add_i32 s2, s27, 0
	ds_read_b128 v[102:105], v11
	ds_read_b128 v[106:109], v16
	v_add_u32_e32 v11, s2, v155
	v_add_u32_e32 v16, s2, v156
	ds_read_b128 v[114:117], v11
	ds_read_b128 v[118:121], v16
	v_add_u32_e32 v11, s2, v157
	v_add_u32_e32 v16, s2, v158
	ds_read_b128 v[122:125], v11
	ds_read_b128 v[182:185], v16
	s_waitcnt lgkmcnt(14)
	v_mfma_f32_16x16x32_bf16 v[2:5], v[2:5], v[50:53], 0
	v_mfma_f32_16x16x32_bf16 v[2:5], v[6:9], v[54:57], v[2:5]
	s_waitcnt lgkmcnt(13)
	v_mfma_f32_16x16x32_bf16 v[2:5], v[12:15], v[58:61], v[2:5]
	s_waitcnt lgkmcnt(12)
	v_mfma_f32_16x16x32_bf16 v[98:101], v[66:69], v[62:65], v[2:5]
	s_waitcnt lgkmcnt(11)
	v_mfma_f32_16x16x32_bf16 v[2:5], v[70:73], v[50:53], 0
	s_waitcnt lgkmcnt(10)
	v_mfma_f32_16x16x32_bf16 v[2:5], v[74:77], v[54:57], v[2:5]
	s_waitcnt lgkmcnt(9)
	v_mfma_f32_16x16x32_bf16 v[2:5], v[78:81], v[58:61], v[2:5]
	s_waitcnt lgkmcnt(8)
	v_mfma_f32_16x16x32_bf16 v[86:89], v[82:85], v[62:65], v[2:5]
	s_xor_b32 s2, s7, s70
	s_lshl_b32 s2, s2, 12
	s_add_i32 s6, s2, 0
	s_nop 2
	v_add_u32_e32 v2, s6, v155
	v_add_u32_e32 v6, s6, v156
	v_add_u32_e32 v11, s6, v157
	v_add_u32_e32 v16, s6, v158
	s_xor_b32 s6, s7, s71
	s_lshl_b32 s56, s6, 12
	s_add_i32 s6, s56, 0
	ds_read_b128 v[2:5], v2
	ds_read_b128 v[6:9], v6
	ds_read_b128 v[12:15], v11
	ds_read_b128 v[66:69], v16
	v_add_u32_e32 v11, s6, v155
	v_add_u32_e32 v16, s6, v156
	ds_read_b128 v[70:73], v11
	ds_read_b128 v[74:77], v16
	v_add_u32_e32 v11, s6, v157
	v_add_u32_e32 v16, s6, v158
	ds_read_b128 v[78:81], v11
	ds_read_b128 v[82:85], v16
	s_waitcnt lgkmcnt(14)
	v_mfma_f32_16x16x32_bf16 v[90:93], v[90:93], v[50:53], 0
	v_mfma_f32_16x16x32_bf16 v[90:93], v[94:97], v[54:57], v[90:93]
	s_waitcnt lgkmcnt(13)
	v_mfma_f32_16x16x32_bf16 v[90:93], v[102:105], v[58:61], v[90:93]
	s_waitcnt lgkmcnt(12)
	v_mfma_f32_16x16x32_bf16 v[110:113], v[106:109], v[62:65], v[90:93]
	s_waitcnt lgkmcnt(11)
	v_mfma_f32_16x16x32_bf16 v[90:93], v[114:117], v[50:53], 0
	s_waitcnt lgkmcnt(10)
	v_mfma_f32_16x16x32_bf16 v[90:93], v[118:121], v[54:57], v[90:93]
	s_waitcnt lgkmcnt(9)
	v_mfma_f32_16x16x32_bf16 v[90:93], v[122:125], v[58:61], v[90:93]
	s_waitcnt lgkmcnt(8)
	v_mfma_f32_16x16x32_bf16 v[94:97], v[182:185], v[62:65], v[90:93]
	s_xor_b32 s6, s7, s74
	s_lshl_b32 s10, s6, 12
	s_add_i32 s6, s10, 0
	v_add_u32_e32 v11, s6, v155
	v_add_u32_e32 v16, s6, v156
	s_nop 0
	ds_read_b128 v[90:93], v11
	ds_read_b128 v[106:109], v16
	v_add_u32_e32 v11, s6, v157
	v_add_u32_e32 v16, s6, v158
	s_xor_b32 s6, s7, s75
	s_lshl_b32 s33, s6, 12
	s_add_i32 s6, s33, 0
	ds_read_b128 v[118:121], v11
	ds_read_b128 v[122:125], v16
	v_add_u32_e32 v11, s6, v155
	v_add_u32_e32 v16, s6, v156
	ds_read_b128 v[182:185], v11
	ds_read_b128 v[186:189], v16
	v_add_u32_e32 v11, s6, v157
	v_add_u32_e32 v16, s6, v158
	ds_read_b128 v[190:193], v11
	ds_read_b128 v[194:197], v16
	s_waitcnt lgkmcnt(14)
	v_mfma_f32_16x16x32_bf16 v[2:5], v[2:5], v[50:53], 0
	v_mfma_f32_16x16x32_bf16 v[2:5], v[6:9], v[54:57], v[2:5]
	s_waitcnt lgkmcnt(13)
	v_mfma_f32_16x16x32_bf16 v[2:5], v[12:15], v[58:61], v[2:5]
	s_waitcnt lgkmcnt(12)
	v_mfma_f32_16x16x32_bf16 v[114:117], v[66:69], v[62:65], v[2:5]
	s_waitcnt lgkmcnt(11)
	v_mfma_f32_16x16x32_bf16 v[2:5], v[70:73], v[50:53], 0
	s_waitcnt lgkmcnt(10)
	v_mfma_f32_16x16x32_bf16 v[2:5], v[74:77], v[54:57], v[2:5]
	s_waitcnt lgkmcnt(9)
	v_mfma_f32_16x16x32_bf16 v[2:5], v[78:81], v[58:61], v[2:5]
	s_waitcnt lgkmcnt(8)
	v_mfma_f32_16x16x32_bf16 v[102:105], v[82:85], v[62:65], v[2:5]
	s_xor_b32 s6, s7, s82
	s_lshl_b32 s6, s6, 12
	s_xor_b32 s7, s7, s83
	s_add_i32 s97, s6, 0
	s_lshl_b32 s7, s7, 12
	s_nop 0
	v_add_u32_e32 v2, s97, v155
	v_add_u32_e32 v6, s97, v156
	v_add_u32_e32 v11, s97, v157
	v_add_u32_e32 v16, s97, v158
	s_add_i32 s97, s7, 0
	ds_read_b128 v[2:5], v2
	ds_read_b128 v[6:9], v6
	ds_read_b128 v[12:15], v11
	ds_read_b128 v[66:69], v16
	v_add_u32_e32 v11, s97, v155
	v_add_u32_e32 v16, s97, v156
	ds_read_b128 v[70:73], v11
	ds_read_b128 v[74:77], v16
	v_add_u32_e32 v11, s97, v157
	v_add_u32_e32 v16, s97, v158
	ds_read_b128 v[78:81], v11
	ds_read_b128 v[82:85], v16
	s_waitcnt lgkmcnt(14)
	v_mfma_f32_16x16x32_bf16 v[90:93], v[90:93], v[50:53], 0
	v_mfma_f32_16x16x32_bf16 v[90:93], v[106:109], v[54:57], v[90:93]
	s_waitcnt lgkmcnt(13)
	v_mfma_f32_16x16x32_bf16 v[90:93], v[118:121], v[58:61], v[90:93]
	s_waitcnt lgkmcnt(12)
	v_mfma_f32_16x16x32_bf16 v[122:125], v[122:125], v[62:65], v[90:93]
	s_waitcnt lgkmcnt(11)
	v_mfma_f32_16x16x32_bf16 v[90:93], v[182:185], v[50:53], 0
	s_waitcnt lgkmcnt(10)
	v_mfma_f32_16x16x32_bf16 v[90:93], v[186:189], v[54:57], v[90:93]
	s_waitcnt lgkmcnt(9)
	v_mfma_f32_16x16x32_bf16 v[90:93], v[190:193], v[58:61], v[90:93]
	s_waitcnt lgkmcnt(8)
	v_mfma_f32_16x16x32_bf16 v[118:121], v[194:197], v[62:65], v[90:93]
	s_waitcnt lgkmcnt(7)
	v_mfma_f32_16x16x32_bf16 v[2:5], v[2:5], v[50:53], 0
	s_waitcnt lgkmcnt(6)
	v_mfma_f32_16x16x32_bf16 v[2:5], v[6:9], v[54:57], v[2:5]
	s_waitcnt lgkmcnt(5)
	v_mfma_f32_16x16x32_bf16 v[2:5], v[12:15], v[58:61], v[2:5]
	s_waitcnt lgkmcnt(4)
	v_mfma_f32_16x16x32_bf16 v[106:109], v[66:69], v[62:65], v[2:5]
	s_waitcnt lgkmcnt(3)
	v_mfma_f32_16x16x32_bf16 v[2:5], v[70:73], v[50:53], 0
	s_waitcnt lgkmcnt(2)
	v_mfma_f32_16x16x32_bf16 v[2:5], v[74:77], v[54:57], v[2:5]
	s_waitcnt lgkmcnt(1)
	v_mfma_f32_16x16x32_bf16 v[2:5], v[78:81], v[58:61], v[2:5]
	s_waitcnt lgkmcnt(0)
	v_mfma_f32_16x16x32_bf16 v[90:93], v[82:85], v[62:65], v[2:5]
	s_add_i32 s57, s88, s57
	s_add_i32 s58, s88, s58
	s_nop 3
	v_add_u32_e32 v2, s57, v159
	v_add_u32_e32 v3, s58, v159
	v_add_u32_e32 v4, s57, v160
	v_add_u32_e32 v5, s58, v160
	v_add_u32_e32 v6, s57, v161
	v_add_u32_e32 v7, s58, v161
	v_add_u32_e32 v8, s57, v162
	v_add_u32_e32 v9, s58, v162
	v_add_u32_e32 v11, s57, v163
	v_add_u32_e32 v12, s58, v163
	v_add_u32_e32 v13, s57, v164
	v_add_u32_e32 v14, s58, v164
	ds_read_b64_tr_b16 v[70:71], v2
	ds_read_b64_tr_b16 v[72:73], v3
	ds_read_b64_tr_b16 v[2:3], v4
	ds_read_b64_tr_b16 v[4:5], v5
	ds_read_b64_tr_b16 v[74:75], v6
	ds_read_b64_tr_b16 v[76:77], v7
	ds_read_b64_tr_b16 v[6:7], v8
	ds_read_b64_tr_b16 v[8:9], v9
	ds_read_b64_tr_b16 v[78:79], v11
	ds_read_b64_tr_b16 v[80:81], v12
	ds_read_b64_tr_b16 v[12:13], v13
	ds_read_b64_tr_b16 v[14:15], v14
	v_add_u32_e32 v11, s57, v165
	v_add_u32_e32 v68, s58, v166
	v_add_u32_e32 v16, s58, v165
	v_add_u32_e32 v17, s57, v166
	ds_read_b64_tr_b16 v[82:83], v11
	ds_read_b64_tr_b16 v[84:85], v16
	ds_read_b64_tr_b16 v[66:67], v17
	ds_read_b64_tr_b16 v[68:69], v68
	s_andn2_b64 vcc, exec, s[54:55]
	s_cbranch_vccnz .LBB0_1098
	s_add_i32 s54, s62, s12
	s_ashr_i32 s55, s54, 31
	s_lshl_b64 s[54:55], s[54:55], s92
	s_add_u32 s54, s54, s18
	s_addc_u32 s55, s55, s19
	s_mul_i32 s57, s55, 0x1800
	v_mad_u64_u32 v[16:17], s[54:55], s54, v180, v[146:147]
	v_add_u32_e32 v17, s57, v17
	global_load_dwordx4 v[50:53], v[16:17], off
	global_load_dwordx4 v[54:57], v[16:17], off offset:64
	global_load_dwordx4 v[58:61], v[16:17], off offset:128
	global_load_dwordx4 v[62:65], v[16:17], off offset:192

.Lattn_slow_join1:
	s_waitcnt vmcnt(0)
	s_branch .LBB0_1070
.Lattn_slow_join2:
	s_waitcnt vmcnt(1)
	s_branch .LBB0_1096
